# proj-GEMM epilogue rotary path (both layers): the 14 later cos/sin vector loads hoisted to the path top into dead registers, counted vmcnt waits instead of a drain per row group
# baseline (speedup 1.0000x reference)
.LBB0_278:
	v_lshlrev_b32_e32 v136, 8, v158
	v_and_b32_e32 v136, 0xfcf00, v136
	v_lshl_add_u64 v[146:147], v[140:141], 0, v[136:137]
	global_load_dwordx4 v[160:163], v[146:147], off
	v_lshl_add_u64 v[146:147], v[138:139], 0, v[136:137]
	global_load_dwordx4 v[164:167], v[146:147], off
	v_mov_b32_e32 v245, 0
	v_lshl_add_u32 v248, v158, 6, v156
	v_and_b32_e32 v248, 0x3f3c0, v248
	v_lshlrev_b32_e32 v248, 2, v248
	v_or_b32_e32 v244, 0x1000, v136
	v_lshl_add_u64 v[246:247], v[140:141], 0, v[244:245]
	global_load_dwordx4 v[180:183], v[246:247], off
	v_lshl_add_u64 v[246:247], v[138:139], 0, v[244:245]
	global_load_dwordx4 v[184:187], v[246:247], off
	v_or_b32_e32 v244, 0x2000, v136
	v_lshl_add_u64 v[246:247], v[140:141], 0, v[244:245]
	global_load_dwordx4 v[188:191], v[246:247], off
	v_lshl_add_u64 v[246:247], v[138:139], 0, v[244:245]
	global_load_dwordx4 v[192:195], v[246:247], off
	v_or_b32_e32 v244, 0x3000, v136
	v_lshl_add_u64 v[246:247], v[140:141], 0, v[244:245]
	global_load_dwordx4 v[196:199], v[246:247], off
	v_lshl_add_u64 v[246:247], v[138:139], 0, v[244:245]
	global_load_dwordx4 v[200:203], v[246:247], off
	v_mov_b32_e32 v244, v248
	v_lshl_add_u64 v[246:247], v[140:141], 0, v[244:245]
	global_load_dwordx4 v[204:207], v[246:247], off
	v_lshl_add_u64 v[246:247], v[138:139], 0, v[244:245]
	global_load_dwordx4 v[208:211], v[246:247], off
	v_or_b32_e32 v244, 0x1000, v248
	v_lshl_add_u64 v[246:247], v[140:141], 0, v[244:245]
	global_load_dwordx4 v[212:215], v[246:247], off
	v_lshl_add_u64 v[246:247], v[138:139], 0, v[244:245]
	global_load_dwordx4 v[216:219], v[246:247], off
	v_or_b32_e32 v244, 0x2000, v248
	v_lshl_add_u64 v[246:247], v[140:141], 0, v[244:245]
	global_load_dwordx4 v[220:223], v[246:247], off
	v_lshl_add_u64 v[246:247], v[138:139], 0, v[244:245]
	global_load_dwordx4 v[224:227], v[246:247], off
	v_or_b32_e32 v244, 0x3000, v248
	v_lshl_add_u64 v[246:247], v[140:141], 0, v[244:245]
	global_load_dwordx4 v[228:231], v[246:247], off
	v_lshl_add_u64 v[246:247], v[138:139], 0, v[244:245]
	global_load_dwordx4 v[232:235], v[246:247], off
	v_mov_b32_e32 v147, v137
	v_or_b32_e32 v146, 0x1000, v136
	v_lshl_add_u64 v[148:149], v[140:141], 0, v[146:147]
	s_waitcnt vmcnt(14)
	v_pk_mul_f32 v[168:169], v[114:115], v[162:163]
	v_pk_mul_f32 v[170:171], v[112:113], v[160:161]
	v_pk_mul_f32 v[172:173], v[118:119], v[162:163]
	v_pk_mul_f32 v[174:175], v[116:117], v[160:161]
	v_pk_mul_f32 v[176:177], v[122:123], v[162:163]
	v_pk_mul_f32 v[178:179], v[120:121], v[160:161]
	v_pk_mul_f32 v[162:163], v[126:127], v[162:163]
	v_pk_mul_f32 v[160:161], v[124:125], v[160:161]
	v_pk_fma_f32 v[118:119], v[118:119], v[166:167], v[168:169] neg_lo:[0,0,1] neg_hi:[0,0,1]
	v_pk_fma_f32 v[116:117], v[116:117], v[164:165], v[170:171] neg_lo:[0,0,1] neg_hi:[0,0,1]
	v_pk_fma_f32 v[168:169], v[114:115], v[166:167], v[172:173]
	v_pk_fma_f32 v[114:115], v[112:113], v[164:165], v[174:175]
	v_pk_fma_f32 v[124:125], v[124:125], v[164:165], v[178:179] neg_lo:[0,0,1] neg_hi:[0,0,1]
	v_pk_fma_f32 v[122:123], v[122:123], v[166:167], v[162:163]
	v_pk_fma_f32 v[120:121], v[120:121], v[164:165], v[160:161]
	v_pk_fma_f32 v[126:127], v[126:127], v[166:167], v[176:177] neg_lo:[0,0,1] neg_hi:[0,0,1]
	v_cvt_pk_bf16_f32 v112, v116, v117
	v_cvt_pk_bf16_f32 v113, v118, v119
	v_cvt_pk_bf16_f32 v114, v114, v115
	v_cvt_pk_bf16_f32 v115, v168, v169
	v_cvt_pk_bf16_f32 v116, v124, v125
	s_nop 0
	v_cvt_pk_bf16_f32 v117, v126, v127
	v_cvt_pk_bf16_f32 v118, v120, v121
	v_cvt_pk_bf16_f32 v119, v122, v123
	v_lshl_add_u64 v[124:125], v[138:139], 0, v[146:147]
	v_or_b32_e32 v146, 0x2000, v136
	v_lshl_add_u64 v[148:149], v[140:141], 0, v[146:147]
	v_or_b32_e32 v136, 0x3000, v136
	s_waitcnt vmcnt(12)
	v_pk_mul_f32 v[160:161], v[98:99], v[182:183]
	v_pk_mul_f32 v[162:163], v[96:97], v[180:181]
	v_pk_mul_f32 v[164:165], v[102:103], v[182:183]
	v_pk_mul_f32 v[166:167], v[100:101], v[180:181]
	v_pk_mul_f32 v[168:169], v[106:107], v[182:183]
	v_pk_mul_f32 v[170:171], v[104:105], v[180:181]
	v_pk_mul_f32 v[122:123], v[110:111], v[182:183]
	v_pk_mul_f32 v[120:121], v[108:109], v[180:181]
	v_pk_fma_f32 v[102:103], v[102:103], v[186:187], v[160:161] neg_lo:[0,0,1] neg_hi:[0,0,1]
	v_pk_fma_f32 v[100:101], v[100:101], v[184:185], v[162:163] neg_lo:[0,0,1] neg_hi:[0,0,1]
	v_pk_fma_f32 v[160:161], v[98:99], v[186:187], v[164:165]
	v_pk_fma_f32 v[98:99], v[96:97], v[184:185], v[166:167]
	v_pk_fma_f32 v[108:109], v[108:109], v[184:185], v[170:171] neg_lo:[0,0,1] neg_hi:[0,0,1]
	v_pk_fma_f32 v[106:107], v[106:107], v[186:187], v[122:123]
	v_pk_fma_f32 v[104:105], v[104:105], v[184:185], v[120:121]
	v_pk_fma_f32 v[110:111], v[110:111], v[186:187], v[168:169] neg_lo:[0,0,1] neg_hi:[0,0,1]
	v_cvt_pk_bf16_f32 v96, v100, v101
	v_cvt_pk_bf16_f32 v97, v102, v103
	v_cvt_pk_bf16_f32 v98, v98, v99
	v_cvt_pk_bf16_f32 v99, v160, v161
	v_cvt_pk_bf16_f32 v100, v108, v109
	s_nop 0
	v_cvt_pk_bf16_f32 v101, v110, v111
	v_cvt_pk_bf16_f32 v102, v104, v105
	v_cvt_pk_bf16_f32 v103, v106, v107
	v_lshl_add_u64 v[108:109], v[138:139], 0, v[146:147]
	v_lshl_add_u64 v[120:121], v[140:141], 0, v[136:137]
	s_waitcnt vmcnt(10)
	v_pk_mul_f32 v[122:123], v[82:83], v[190:191]
	v_pk_mul_f32 v[124:125], v[80:81], v[188:189]
	v_pk_mul_f32 v[126:127], v[86:87], v[190:191]
	v_pk_mul_f32 v[146:147], v[84:85], v[188:189]
	v_pk_mul_f32 v[148:149], v[90:91], v[190:191]
	v_pk_mul_f32 v[160:161], v[88:89], v[188:189]
	v_pk_mul_f32 v[106:107], v[94:95], v[190:191]
	v_pk_mul_f32 v[104:105], v[92:93], v[188:189]
	v_pk_fma_f32 v[86:87], v[86:87], v[194:195], v[122:123] neg_lo:[0,0,1] neg_hi:[0,0,1]
	v_pk_fma_f32 v[84:85], v[84:85], v[192:193], v[124:125] neg_lo:[0,0,1] neg_hi:[0,0,1]
	v_pk_fma_f32 v[122:123], v[82:83], v[194:195], v[126:127]
	v_pk_fma_f32 v[82:83], v[80:81], v[192:193], v[146:147]
	v_pk_fma_f32 v[92:93], v[92:93], v[192:193], v[160:161] neg_lo:[0,0,1] neg_hi:[0,0,1]
	v_pk_fma_f32 v[90:91], v[90:91], v[194:195], v[106:107]
	v_pk_fma_f32 v[88:89], v[88:89], v[192:193], v[104:105]
	v_pk_fma_f32 v[94:95], v[94:95], v[194:195], v[148:149] neg_lo:[0,0,1] neg_hi:[0,0,1]
	v_cvt_pk_bf16_f32 v80, v84, v85
	v_cvt_pk_bf16_f32 v81, v86, v87
	v_cvt_pk_bf16_f32 v82, v82, v83
	v_cvt_pk_bf16_f32 v83, v122, v123
	v_cvt_pk_bf16_f32 v84, v92, v93
	s_nop 0
	v_cvt_pk_bf16_f32 v85, v94, v95
	v_cvt_pk_bf16_f32 v86, v88, v89
	v_cvt_pk_bf16_f32 v87, v90, v91
	v_lshl_add_u64 v[92:93], v[138:139], 0, v[136:137]
	v_lshl_add_u32 v104, v158, 6, v156
	v_and_b32_e32 v104, 0x3f3c0, v104
	v_add_u32_e32 v126, 0x5a000, v157
	v_add_u32_e32 v127, 0xb4000, v157
	v_add_u32_e32 v146, 0x10e000, v157
	v_lshlrev_b32_e32 v136, 2, v104
	v_lshl_add_u64 v[104:105], v[140:141], 0, v[136:137]
	s_waitcnt vmcnt(8)
	v_pk_mul_f32 v[106:107], v[66:67], v[198:199]
	v_pk_mul_f32 v[108:109], v[64:65], v[196:197]
	v_pk_mul_f32 v[110:111], v[70:71], v[198:199]
	v_pk_mul_f32 v[120:121], v[68:69], v[196:197]
	v_pk_mul_f32 v[122:123], v[74:75], v[198:199]
	v_pk_mul_f32 v[124:125], v[72:73], v[196:197]
	v_pk_mul_f32 v[90:91], v[78:79], v[198:199]
	v_pk_mul_f32 v[88:89], v[76:77], v[196:197]
	v_pk_fma_f32 v[70:71], v[70:71], v[202:203], v[106:107] neg_lo:[0,0,1] neg_hi:[0,0,1]
	v_pk_fma_f32 v[68:69], v[68:69], v[200:201], v[108:109] neg_lo:[0,0,1] neg_hi:[0,0,1]
	v_pk_fma_f32 v[106:107], v[66:67], v[202:203], v[110:111]
	v_pk_fma_f32 v[66:67], v[64:65], v[200:201], v[120:121]
	v_pk_fma_f32 v[78:79], v[78:79], v[202:203], v[122:123] neg_lo:[0,0,1] neg_hi:[0,0,1]
	v_pk_fma_f32 v[76:77], v[76:77], v[200:201], v[124:125] neg_lo:[0,0,1] neg_hi:[0,0,1]
	v_pk_fma_f32 v[74:75], v[74:75], v[202:203], v[90:91]
	v_pk_fma_f32 v[72:73], v[72:73], v[200:201], v[88:89]
	v_cvt_pk_bf16_f32 v64, v68, v69
	v_cvt_pk_bf16_f32 v65, v70, v71
	v_cvt_pk_bf16_f32 v66, v66, v67
	v_cvt_pk_bf16_f32 v67, v106, v107
	v_cvt_pk_bf16_f32 v68, v76, v77
	v_cvt_pk_bf16_f32 v69, v78, v79
	s_nop 0
	v_cvt_pk_bf16_f32 v70, v72, v73
	v_cvt_pk_bf16_f32 v71, v74, v75
	global_store_dwordx4 v157, v[112:115], s[8:9]
	global_store_dwordx4 v157, v[116:119], s[8:9] offset:256
	global_store_dwordx4 v126, v[96:99], s[8:9]
	global_store_dwordx4 v126, v[100:103], s[8:9] offset:256
	global_store_dwordx4 v127, v[80:83], s[8:9]
	global_store_dwordx4 v127, v[84:87], s[8:9] offset:256
	global_store_dwordx4 v146, v[64:67], s[8:9]
	global_store_dwordx4 v146, v[68:71], s[8:9] offset:256
	v_mov_b32_e32 v73, v137
	v_lshl_add_u64 v[68:69], v[138:139], 0, v[136:137]
	v_or_b32_e32 v72, 0x1000, v136
	v_lshl_add_u64 v[74:75], v[140:141], 0, v[72:73]
	s_waitcnt vmcnt(14)
	v_pk_mul_f32 v[76:77], v[50:51], v[206:207]
	v_pk_mul_f32 v[78:79], v[48:49], v[204:205]
	v_pk_mul_f32 v[80:81], v[54:55], v[206:207]
	v_pk_mul_f32 v[82:83], v[52:53], v[204:205]
	v_pk_mul_f32 v[84:85], v[58:59], v[206:207]
	v_pk_mul_f32 v[86:87], v[56:57], v[204:205]
	v_pk_mul_f32 v[66:67], v[62:63], v[206:207]
	v_pk_mul_f32 v[64:65], v[60:61], v[204:205]
	v_pk_fma_f32 v[54:55], v[54:55], v[210:211], v[76:77] neg_lo:[0,0,1] neg_hi:[0,0,1]
	v_pk_fma_f32 v[52:53], v[52:53], v[208:209], v[78:79] neg_lo:[0,0,1] neg_hi:[0,0,1]
	v_pk_fma_f32 v[76:77], v[50:51], v[210:211], v[80:81]
	v_pk_fma_f32 v[50:51], v[48:49], v[208:209], v[82:83]
	v_pk_fma_f32 v[60:61], v[60:61], v[208:209], v[86:87] neg_lo:[0,0,1] neg_hi:[0,0,1]
	v_pk_fma_f32 v[58:59], v[58:59], v[210:211], v[66:67]
	v_pk_fma_f32 v[56:57], v[56:57], v[208:209], v[64:65]
	v_pk_fma_f32 v[62:63], v[62:63], v[210:211], v[84:85] neg_lo:[0,0,1] neg_hi:[0,0,1]
	v_cvt_pk_bf16_f32 v48, v52, v53
	v_cvt_pk_bf16_f32 v49, v54, v55
	v_cvt_pk_bf16_f32 v50, v50, v51
	v_cvt_pk_bf16_f32 v51, v76, v77
	v_cvt_pk_bf16_f32 v52, v60, v61
	s_nop 0
	v_cvt_pk_bf16_f32 v53, v62, v63
	v_cvt_pk_bf16_f32 v54, v56, v57
	v_cvt_pk_bf16_f32 v55, v58, v59
	v_lshl_add_u64 v[60:61], v[138:139], 0, v[72:73]
	v_mov_b32_e32 v65, v137
	v_or_b32_e32 v64, 0x2000, v136
	v_lshl_add_u64 v[66:67], v[140:141], 0, v[64:65]
	v_or_b32_e32 v136, 0x3000, v136
	s_waitcnt vmcnt(12)
	v_pk_mul_f32 v[68:69], v[34:35], v[214:215]
	v_pk_mul_f32 v[70:71], v[32:33], v[212:213]
	v_pk_mul_f32 v[72:73], v[38:39], v[214:215]
	v_pk_mul_f32 v[74:75], v[36:37], v[212:213]
	v_pk_mul_f32 v[76:77], v[42:43], v[214:215]
	v_pk_mul_f32 v[78:79], v[40:41], v[212:213]
	v_pk_mul_f32 v[58:59], v[46:47], v[214:215]
	v_pk_mul_f32 v[56:57], v[44:45], v[212:213]
	v_pk_fma_f32 v[38:39], v[38:39], v[218:219], v[68:69] neg_lo:[0,0,1] neg_hi:[0,0,1]
	v_pk_fma_f32 v[36:37], v[36:37], v[216:217], v[70:71] neg_lo:[0,0,1] neg_hi:[0,0,1]
	v_pk_fma_f32 v[68:69], v[34:35], v[218:219], v[72:73]
	v_pk_fma_f32 v[34:35], v[32:33], v[216:217], v[74:75]
	v_pk_fma_f32 v[44:45], v[44:45], v[216:217], v[78:79] neg_lo:[0,0,1] neg_hi:[0,0,1]
	v_pk_fma_f32 v[42:43], v[42:43], v[218:219], v[58:59]
	v_pk_fma_f32 v[40:41], v[40:41], v[216:217], v[56:57]
	v_pk_fma_f32 v[46:47], v[46:47], v[218:219], v[76:77] neg_lo:[0,0,1] neg_hi:[0,0,1]
	v_cvt_pk_bf16_f32 v32, v36, v37
	v_cvt_pk_bf16_f32 v33, v38, v39
	v_cvt_pk_bf16_f32 v34, v34, v35
	v_cvt_pk_bf16_f32 v35, v68, v69
	v_cvt_pk_bf16_f32 v36, v44, v45
	s_nop 0
	v_cvt_pk_bf16_f32 v37, v46, v47
	v_cvt_pk_bf16_f32 v38, v40, v41
	v_cvt_pk_bf16_f32 v39, v42, v43
	v_lshl_add_u64 v[44:45], v[138:139], 0, v[64:65]
	v_lshl_add_u64 v[56:57], v[140:141], 0, v[136:137]
	s_waitcnt vmcnt(10)
	v_pk_mul_f32 v[58:59], v[18:19], v[222:223]
	v_pk_mul_f32 v[60:61], v[16:17], v[220:221]
	v_pk_mul_f32 v[62:63], v[22:23], v[222:223]
	v_pk_mul_f32 v[64:65], v[20:21], v[220:221]
	v_pk_mul_f32 v[66:67], v[26:27], v[222:223]
	v_pk_mul_f32 v[68:69], v[24:25], v[220:221]
	v_pk_mul_f32 v[42:43], v[30:31], v[222:223]
	v_pk_mul_f32 v[40:41], v[28:29], v[220:221]
	v_pk_fma_f32 v[22:23], v[22:23], v[226:227], v[58:59] neg_lo:[0,0,1] neg_hi:[0,0,1]
	v_pk_fma_f32 v[20:21], v[20:21], v[224:225], v[60:61] neg_lo:[0,0,1] neg_hi:[0,0,1]
	v_pk_fma_f32 v[58:59], v[18:19], v[226:227], v[62:63]
	v_pk_fma_f32 v[18:19], v[16:17], v[224:225], v[64:65]
	v_pk_fma_f32 v[28:29], v[28:29], v[224:225], v[68:69] neg_lo:[0,0,1] neg_hi:[0,0,1]
	v_pk_fma_f32 v[26:27], v[26:27], v[226:227], v[42:43]
	v_pk_fma_f32 v[24:25], v[24:25], v[224:225], v[40:41]
	v_pk_fma_f32 v[30:31], v[30:31], v[226:227], v[66:67] neg_lo:[0,0,1] neg_hi:[0,0,1]
	v_cvt_pk_bf16_f32 v16, v20, v21
	v_cvt_pk_bf16_f32 v17, v22, v23
	v_cvt_pk_bf16_f32 v18, v18, v19
	v_cvt_pk_bf16_f32 v19, v58, v59
	v_cvt_pk_bf16_f32 v20, v28, v29
	s_nop 0
	v_cvt_pk_bf16_f32 v21, v30, v31
	v_cvt_pk_bf16_f32 v22, v24, v25
	v_cvt_pk_bf16_f32 v23, v26, v27
	v_lshl_add_u64 v[28:29], v[138:139], 0, v[136:137]
	v_add_u32_e32 v60, 0x2d0000, v157
	v_add_u32_e32 v61, 0x32a000, v157
	v_add_u32_e32 v62, 0x384000, v157
	v_add_u32_e32 v63, 0x3de000, v157
	s_waitcnt vmcnt(8)
	v_pk_mul_f32 v[40:41], v[2:3], v[230:231]
	v_pk_mul_f32 v[42:43], v[0:1], v[228:229]
	v_pk_mul_f32 v[44:45], v[6:7], v[230:231]
	v_pk_mul_f32 v[46:47], v[4:5], v[228:229]
	v_pk_mul_f32 v[56:57], v[10:11], v[230:231]
	v_pk_mul_f32 v[58:59], v[8:9], v[228:229]
	v_pk_mul_f32 v[26:27], v[14:15], v[230:231]
	v_pk_mul_f32 v[24:25], v[12:13], v[228:229]
	v_pk_fma_f32 v[6:7], v[6:7], v[234:235], v[40:41] neg_lo:[0,0,1] neg_hi:[0,0,1]
	v_pk_fma_f32 v[4:5], v[4:5], v[232:233], v[42:43] neg_lo:[0,0,1] neg_hi:[0,0,1]
	v_pk_fma_f32 v[40:41], v[2:3], v[234:235], v[44:45]
	v_pk_fma_f32 v[2:3], v[0:1], v[232:233], v[46:47]
	v_pk_fma_f32 v[14:15], v[14:15], v[234:235], v[56:57] neg_lo:[0,0,1] neg_hi:[0,0,1]
	v_pk_fma_f32 v[12:13], v[12:13], v[232:233], v[58:59] neg_lo:[0,0,1] neg_hi:[0,0,1]
	v_pk_fma_f32 v[10:11], v[10:11], v[234:235], v[26:27]
	v_pk_fma_f32 v[8:9], v[8:9], v[232:233], v[24:25]
	v_cvt_pk_bf16_f32 v0, v4, v5
	v_cvt_pk_bf16_f32 v1, v6, v7
	v_cvt_pk_bf16_f32 v2, v2, v3
	v_cvt_pk_bf16_f32 v3, v40, v41
	v_cvt_pk_bf16_f32 v4, v12, v13
	v_cvt_pk_bf16_f32 v5, v14, v15
	s_nop 0
	v_cvt_pk_bf16_f32 v6, v8, v9
	v_cvt_pk_bf16_f32 v7, v10, v11
	global_store_dwordx4 v60, v[48:51], s[8:9]
	global_store_dwordx4 v60, v[52:55], s[8:9] offset:256
	global_store_dwordx4 v61, v[32:35], s[8:9]
	global_store_dwordx4 v61, v[36:39], s[8:9] offset:256
	global_store_dwordx4 v62, v[16:19], s[8:9]
	global_store_dwordx4 v62, v[20:23], s[8:9] offset:256
	global_store_dwordx4 v63, v[0:3], s[8:9]
	global_store_dwordx4 v63, v[4:7], s[8:9] offset:256
	s_andn2_b64 vcc, exec, s[2:3]
	s_mov_b64 s[2:3], -1
	s_cbranch_vccnz .LBB0_267
